# MoE unit lookup: 24-bit multiplies instead of 32-bit (small table values)
# baseline (speedup 1.0000x reference)
.LBB0_992:
	s_andn2_b64 vcc, exec, s[4:5]
	s_cbranch_vccnz .LBB0_1013
	v_bfe_i32 v4, v6, 27, 1
	v_lshlrev_b32_e32 v3, 4, v6
	v_lshrrev_b32_e32 v4, 22, v4
	v_add_u32_e32 v4, v3, v4
	v_and_b32_e32 v4, 0xfffffc00, v4
	v_sub_u32_e32 v4, v3, v4
	v_lshrrev_b32_e32 v5, 4, v4
	v_bitop3_b32 v4, v5, v4, 32 bitop3:0x6c
	v_ashrrev_i32_e32 v7, 31, v4
	v_ashrrev_i32_e32 v2, 31, v6
	v_lshrrev_b32_e32 v7, 26, v7
	v_lshrrev_b32_e32 v2, 26, v2
	v_add_u32_e32 v7, v4, v7
	v_add_u32_e32 v2, v6, v2
	v_ashrrev_i32_e32 v8, 6, v7
	v_and_b32_e32 v7, 0xc0, v7
	v_ashrrev_i32_e32 v2, 6, v2
	v_sub_u32_e32 v4, v4, v7
	v_lshlrev_b32_e32 v5, 3, v2
	v_lshlrev_b32_e32 v2, 5, v2
	v_ashrrev_i16_sdwa v4, v197, sext(v4) dst_sel:DWORD dst_unused:UNUSED_PAD src0_sel:DWORD src1_sel:BYTE_0
	v_and_b32_e32 v2, 32, v2
	v_bfe_i32 v4, v4, 0, 16
	v_add_u32_e32 v3, 0x2000, v3
	v_and_b32_e32 v5, -16, v5
	v_add_lshl_u32 v2, v2, v4, 1
	v_ashrrev_i32_e32 v4, 31, v3
	v_add_u32_e32 v5, v8, v5
	v_lshrrev_b32_e32 v4, 22, v4
	v_lshlrev_b32_e32 v7, 1, v5
	v_lshrrev_b32_e32 v9, 2, v5
	v_and_b32_e32 v8, 3, v8
	s_mov_b32 s13, 0x1fffe0
	v_add_u32_e32 v4, v3, v4
	v_and_b32_e32 v7, 24, v7
	v_and_b32_e32 v9, 4, v9
	v_and_or_b32 v8, v5, s13, v8
	v_ashrrev_i32_e32 v4, 10, v4
	v_or3_b32 v8, v8, v9, v7
	v_lshl_add_u32 v7, v5, 11, v2
	v_mul_i32_i24_e32 v5, 0x400, v4
	v_sub_u32_e32 v3, v3, v5
	v_lshrrev_b32_e32 v5, 4, v3
	v_bitop3_b32 v3, v5, v3, 32 bitop3:0x6c
	v_lshl_add_u32 v200, v8, 11, v2
	v_ashrrev_i32_e32 v8, 31, v3
	v_lshrrev_b32_e32 v8, 26, v8
	v_add_u32_e32 v8, v3, v8
	v_lshlrev_b32_e32 v5, 3, v4
	v_ashrrev_i32_e32 v9, 6, v8
	v_and_b32_e32 v8, 0xc0, v8
	v_and_b32_e32 v5, -16, v5
	v_sub_u32_e32 v3, v3, v8
	v_add_u32_e32 v5, v9, v5
	v_lshlrev_b32_e32 v4, 5, v4
	v_ashrrev_i16_sdwa v3, v197, sext(v3) dst_sel:DWORD dst_unused:UNUSED_PAD src0_sel:DWORD src1_sel:BYTE_0
	v_and_b32_e32 v9, 3, v9
	v_and_b32_e32 v4, 32, v4
	v_bfe_i32 v3, v3, 0, 16
	v_lshlrev_b32_e32 v8, 1, v5
	v_lshrrev_b32_e32 v10, 2, v5
	v_and_or_b32 v9, v5, s13, v9
	v_readlane_b32 s13, v254, 61
	v_and_b32_e32 v8, 24, v8
	v_and_b32_e32 v10, 4, v10
	v_add_lshl_u32 v3, v4, v3, 1
	v_mov_b32_e32 v4, s13
	v_or3_b32 v9, v9, v10, v8
	v_lshl_add_u32 v8, v5, 11, v3
	ds_read2_b32 v[4:5], v4 offset1:1
	v_readlane_b32 s13, v254, 62
	v_lshl_add_u32 v202, v9, 11, v3
	v_readlane_b32 s4, v255, 18
	v_readlane_b32 s5, v255, 19
	s_waitcnt lgkmcnt(0)
	v_mul_u32_u24_e32 v4, 11, v4
	v_cmp_ge_i32_e32 vcc, s10, v4
	v_mul_u32_u24_e32 v4, 11, v5
	s_mul_hi_i32 s6, s4, 0x5800000
	v_cndmask_b32_e64 v9, 0, 1, vcc
	v_cmp_ge_i32_e32 vcc, s10, v4
	v_mov_b32_e32 v4, s13
	ds_read2_b32 v[4:5], v4 offset1:1
	v_cndmask_b32_e64 v10, 0, 1, vcc
	v_readlane_b32 s13, v254, 63
	s_mul_i32 s7, s4, 0x5800000
	s_add_u32 s4, s0, 0x2c300000
	s_waitcnt lgkmcnt(0)
	v_mul_u32_u24_e32 v4, 11, v4
	v_cmp_ge_i32_e32 vcc, s10, v4
	v_mul_u32_u24_e32 v4, 11, v5
	s_addc_u32 s5, s1, 0
	v_addc_co_u32_e32 v9, vcc, v10, v9, vcc
	v_cmp_ge_i32_e32 vcc, s10, v4
	v_mov_b32_e32 v4, s13
	ds_read2_b32 v[4:5], v4 offset1:1
	v_cndmask_b32_e64 v10, 0, 1, vcc
	v_readlane_b32 s13, v255, 0
	s_add_u32 s60, s74, s7
	s_addc_u32 s61, s75, s6
	s_waitcnt lgkmcnt(0)
	v_mul_u32_u24_e32 v4, 11, v4
	v_cmp_ge_i32_e32 vcc, s10, v4
	v_mul_u32_u24_e32 v4, 11, v5
	s_add_u32 s6, s0, 0x42700000
	v_addc_co_u32_e32 v9, vcc, v9, v10, vcc
	v_cmp_ge_i32_e32 vcc, s10, v4
	v_mov_b32_e32 v4, s13
	ds_read2_b32 v[4:5], v4 offset1:1
	v_cndmask_b32_e64 v10, 0, 1, vcc
	v_readlane_b32 s13, v255, 1
	s_addc_u32 s7, s1, 0
	s_ashr_i32 s8, s2, 6
	s_waitcnt lgkmcnt(0)
	v_mul_u32_u24_e32 v4, 11, v4
	v_cmp_ge_i32_e32 vcc, s10, v4
	v_mul_u32_u24_e32 v4, 11, v5
	s_ashr_i32 s9, s2, 8
	v_addc_co_u32_e32 v9, vcc, v9, v10, vcc
	v_cmp_ge_i32_e32 vcc, s10, v4
	v_mov_b32_e32 v4, s13
	ds_read2_b32 v[4:5], v4 offset1:1
	v_cndmask_b32_e64 v10, 0, 1, vcc
	v_readlane_b32 s13, v255, 2
	s_lshl_b32 s62, s8, 10
	v_and_b32_e32 v231, 0x7fe, v2
	s_waitcnt lgkmcnt(0)
	v_mul_u32_u24_e32 v4, 11, v4
	v_cmp_ge_i32_e32 vcc, s10, v4
	v_mul_u32_u24_e32 v4, 11, v5
	v_and_b32_e32 v232, 0x7fe, v3
	v_addc_co_u32_e32 v9, vcc, v9, v10, vcc
	v_cmp_ge_i32_e32 vcc, s10, v4
	v_mov_b32_e32 v4, s13
	ds_read2_b32 v[4:5], v4 offset1:1
	v_cndmask_b32_e64 v10, 0, 1, vcc
	v_readlane_b32 s13, v255, 3
	v_mov_b32_e32 v201, v195
	v_mov_b32_e32 v203, v195
	s_waitcnt lgkmcnt(0)
	v_mul_u32_u24_e32 v4, 11, v4
	v_cmp_ge_i32_e32 vcc, s10, v4
	v_mul_u32_u24_e32 v4, 11, v5
	s_nop 0
	v_addc_co_u32_e32 v9, vcc, v9, v10, vcc
	v_cmp_ge_i32_e32 vcc, s10, v4
	v_mov_b32_e32 v4, s13
	ds_read2_b32 v[4:5], v4 offset1:1
	v_cndmask_b32_e64 v10, 0, 1, vcc
	v_readlane_b32 s13, v255, 4
	s_waitcnt lgkmcnt(0)
	v_mul_u32_u24_e32 v4, 11, v4
	v_cmp_ge_i32_e32 vcc, s10, v4
	v_mul_u32_u24_e32 v5, 11, v5
	s_nop 0
	v_addc_co_u32_e32 v4, vcc, v9, v10, vcc
	v_mov_b32_e32 v9, s13
	ds_read_b32 v9, v9
	v_cmp_ge_i32_e32 vcc, s10, v5
	s_waitcnt lgkmcnt(0)
	v_mul_u32_u24_e32 v9, 11, v9
	v_cndmask_b32_e64 v5, 0, 1, vcc
	v_cmp_ge_i32_e32 vcc, s10, v9
	s_nop 1
	v_addc_co_u32_e32 v9, vcc, v4, v5, vcc
	v_lshlrev_b32_e32 v4, 2, v9
	v_add_u32_e32 v4, 0, v4
	v_add_u32_e32 v4, 0x25840, v4
	ds_read2_b32 v[4:5], v4 offset1:1
	s_waitcnt lgkmcnt(0)
	v_sub_u32_e32 v5, v5, v4
	v_sub_u32_e32 v13, 0, v5
	v_max_i32_e32 v13, v5, v13
	v_cvt_f32_u32_e32 v14, v13
	v_mul_lo_u32 v10, v4, -11
	v_sub_u32_e32 v15, 0, v13
	v_add_u32_e32 v11, s10, v10
	v_rcp_iflag_f32_e32 v14, v14
	v_sub_u32_e32 v12, 0, v11
	v_max_i32_e32 v12, v11, v12
	v_xor_b32_e32 v10, v11, v5
	v_mul_f32_e32 v14, 0x4f7ffffe, v14
	v_cvt_u32_f32_e32 v14, v14
	v_ashrrev_i32_e32 v10, 31, v10
	v_add_u32_e32 v4, v11, v4
	s_mov_b32 s10, 0x580000
	v_mul_lo_u32 v15, v15, v14
	v_mul_hi_u32 v15, v14, v15
	v_add_u32_e32 v14, v14, v15
	v_mul_hi_u32 v14, v12, v14
	v_mul_lo_u32 v15, v14, v13
	v_sub_u32_e32 v12, v12, v15
	v_add_u32_e32 v15, 1, v14
	v_sub_u32_e32 v16, v12, v13
	v_cmp_ge_u32_e32 vcc, v12, v13
	s_nop 1
	v_cndmask_b32_e32 v14, v14, v15, vcc
	v_cndmask_b32_e32 v12, v12, v16, vcc
	v_add_u32_e32 v15, 1, v14
	v_cmp_ge_u32_e32 vcc, v12, v13
	s_nop 1
	v_cndmask_b32_e32 v12, v14, v15, vcc
	v_xor_b32_e32 v12, v12, v10
	v_sub_u32_e32 v10, v12, v10
	v_mul_lo_u32 v5, v10, v5
	v_sub_u32_e32 v14, v4, v5
	v_mul_hi_u32 v5, v9, s10
	v_mul_lo_u32 v4, v9, s10
	v_readfirstlane_b32 s10, v14
	v_ashrrev_i32_e32 v11, 31, v10
	s_lshl_b32 s10, s10, 8
	v_lshrrev_b32_e32 v9, 11, v7
	v_lshlrev_b64 v[12:13], 19, v[10:11]
	v_readfirstlane_b32 s13, v10
	v_add_u32_e32 v10, s10, v9
	v_ashrrev_i32_e32 v11, 31, v10
	v_lshl_add_u64 v[4:5], v[4:5], 0, v[12:13]
	v_lshl_add_u64 v[10:11], v[10:11], 2, s[6:7]
	v_lshrrev_b32_e32 v13, 11, v8
	global_load_dword v12, v[10:11], off
	v_add_u32_e32 v10, s10, v13
	v_ashrrev_i32_e32 v11, 31, v10
	v_lshl_add_u64 v[10:11], v[10:11], 2, s[6:7]
	s_or_b32 s14, s10, 0x80
	global_load_dword v14, v[10:11], off
	v_add_u32_e32 v10, s14, v9
	v_ashrrev_i32_e32 v11, 31, v10
	v_lshl_add_u64 v[10:11], v[10:11], 2, s[6:7]
	global_load_dword v9, v[10:11], off
	v_add_u32_e32 v10, s14, v13
	v_ashrrev_i32_e32 v11, 31, v10
	v_lshl_add_u64 v[10:11], v[10:11], 2, s[6:7]
	global_load_dword v10, v[10:11], off
	v_readfirstlane_b32 s16, v4
	v_readfirstlane_b32 s14, v5
	s_add_u32 s26, s60, s16
	s_addc_u32 s27, s61, s14
	s_add_i32 s63, s62, 0
	s_add_i32 s64, s63, 0x10000
	s_mov_b32 m0, s64
	s_add_i32 s65, s63, 0x12000
	global_load_lds_dwordx4 v200, s[26:27]
	s_mov_b32 m0, s65
	s_add_i32 s66, s63, 0x2000
	global_load_lds_dwordx4 v202, s[26:27]
	s_mov_b32 m0, s63
	s_add_u32 s16, s26, 0x40000
	s_addc_u32 s17, s27, 0
	s_add_i32 s67, s63, 0x4000
	s_add_i32 s68, s63, 0x6000
	v_lshl_add_u64 v[2:3], s[26:27], 0, v[200:201]
	v_lshl_add_u64 v[4:5], s[26:27], 0, v[202:203]
	s_waitcnt vmcnt(0)
	v_lshl_or_b32 v194, v12, 11, v231
	global_load_lds_dwordx4 v194, s[4:5]
	s_mov_b32 m0, s66
	v_lshl_or_b32 v204, v14, 11, v232
	global_load_lds_dwordx4 v204, s[4:5]
	s_add_i32 m0, s63, 0x14000
	v_lshl_or_b32 v208, v9, 11, v231
	global_load_lds_dwordx4 v200, s[16:17]
	s_add_i32 m0, s63, 0x16000
	v_lshl_or_b32 v206, v10, 11, v232
	global_load_lds_dwordx4 v202, s[16:17]
	s_mov_b32 m0, s67
	s_cmp_lg_u32 s9, 1
	global_load_lds_dwordx4 v208, s[4:5]
	s_mov_b32 m0, s68
	s_nop 0
	global_load_lds_dwordx4 v206, s[4:5]
	s_cbranch_scc1 .LBB0_995
	s_barrier

.Les_p8_skip:
	v_mov_b32_e32 v4, s44
	v_mov_b64_e32 v[2:3], s[42:43]
	v_mov_b32_e32 v5, s73
	s_cbranch_vccnz .LBB0_1002
	v_readlane_b32 s6, v254, 61
	s_nop 1
	v_mov_b32_e32 v2, s6
	ds_read2_b32 v[2:3], v2 offset1:1
	v_readlane_b32 s6, v254, 62
	s_waitcnt lgkmcnt(0)
	v_mul_u32_u24_e32 v2, 11, v2
	v_mov_b32_e32 v4, s6
	v_readlane_b32 s6, v254, 63
	v_cmp_ge_i32_e32 vcc, s14, v2
	v_mul_u32_u24_e32 v3, 11, v3
	v_mov_b32_e32 v6, s6
	v_readlane_b32 s6, v255, 0
	v_cndmask_b32_e64 v2, 0, 1, vcc
	v_cmp_ge_i32_e32 vcc, s14, v3
	v_mov_b32_e32 v8, s6
	ds_read2_b32 v[4:5], v4 offset1:1
	ds_read2_b32 v[6:7], v6 offset1:1
	ds_read2_b32 v[8:9], v8 offset1:1
	v_cndmask_b32_e64 v3, 0, 1, vcc
	v_readlane_b32 s6, v255, 1
	s_waitcnt lgkmcnt(0)
	v_mul_u32_u24_e32 v4, 11, v4
	v_cmp_ge_i32_e32 vcc, s14, v4
	v_mul_u32_u24_e32 v4, 11, v6
	s_nop 0
	v_addc_co_u32_e32 v2, vcc, v3, v2, vcc
	v_mul_u32_u24_e32 v3, 11, v5
	v_cmp_ge_i32_e32 vcc, s14, v3
	s_nop 1
	v_cndmask_b32_e64 v3, 0, 1, vcc
	v_cmp_ge_i32_e32 vcc, s14, v4
	v_mul_u32_u24_e32 v4, 11, v8
	s_nop 0
	v_addc_co_u32_e32 v2, vcc, v2, v3, vcc
	v_mul_u32_u24_e32 v3, 11, v7
	v_cmp_ge_i32_e32 vcc, s14, v3
	s_nop 1
	v_cndmask_b32_e64 v3, 0, 1, vcc
	v_cmp_ge_i32_e32 vcc, s14, v4
	s_nop 1
	v_addc_co_u32_e32 v8, vcc, v2, v3, vcc
	v_mul_u32_u24_e32 v2, 11, v9
	v_cmp_ge_i32_e32 vcc, s14, v2
	v_mov_b32_e32 v2, s6
	ds_read2_b32 v[2:3], v2 offset1:1
	v_readlane_b32 s6, v255, 2
	v_cndmask_b32_e64 v9, 0, 1, vcc
	s_waitcnt lgkmcnt(0)
	v_mul_u32_u24_e32 v2, 11, v2
	v_mov_b32_e32 v4, s6
	v_readlane_b32 s6, v255, 3
	v_cmp_ge_i32_e32 vcc, s14, v2
	v_mul_u32_u24_e32 v3, 11, v3
	v_mov_b32_e32 v6, s6
	v_readlane_b32 s6, v255, 4
	v_addc_co_u32_e32 v2, vcc, v8, v9, vcc
	s_nop 0
	v_mov_b32_e32 v10, s6
	ds_read2_b32 v[4:5], v4 offset1:1
	ds_read2_b32 v[6:7], v6 offset1:1
	ds_read_b32 v10, v10
	v_cmp_ge_i32_e32 vcc, s14, v3
	s_mov_b32 s6, 0x580000
	s_waitcnt lgkmcnt(0)
	v_mul_u32_u24_e32 v4, 11, v4
	v_cndmask_b32_e64 v3, 0, 1, vcc
	v_cmp_ge_i32_e32 vcc, s14, v4
	v_mul_u32_u24_e32 v4, 11, v6
	s_nop 0
	v_addc_co_u32_e32 v2, vcc, v2, v3, vcc
	v_mul_u32_u24_e32 v3, 11, v5
	v_cmp_ge_i32_e32 vcc, s14, v3
	s_nop 1
	v_cndmask_b32_e64 v3, 0, 1, vcc
	v_cmp_ge_i32_e32 vcc, s14, v4
	v_mul_u32_u24_e32 v4, 11, v10
	s_nop 0
	v_addc_co_u32_e32 v2, vcc, v2, v3, vcc
	v_mul_u32_u24_e32 v3, 11, v7
	v_cmp_ge_i32_e32 vcc, s14, v3
	s_nop 1
	v_cndmask_b32_e64 v3, 0, 1, vcc
	v_cmp_ge_i32_e32 vcc, s14, v4
	s_nop 1
	v_addc_co_u32_e32 v4, vcc, v2, v3, vcc
	v_lshlrev_b32_e32 v2, 2, v4
	v_add_u32_e32 v2, 0, v2
	v_add_u32_e32 v2, 0x25840, v2
	ds_read2_b32 v[2:3], v2 offset1:1
	s_waitcnt lgkmcnt(0)
	v_sub_u32_e32 v3, v3, v2
	v_sub_u32_e32 v5, 0, v3
	v_max_i32_e32 v5, v3, v5
	v_cvt_f32_u32_e32 v6, v5
	v_mul_lo_u32 v7, v2, -11
	v_sub_u32_e32 v10, 0, v5
	v_add_u32_e32 v7, s14, v7
	v_rcp_iflag_f32_e32 v6, v6
	v_sub_u32_e32 v9, 0, v7
	v_max_i32_e32 v9, v7, v9
	v_xor_b32_e32 v8, v7, v3
	v_mul_f32_e32 v6, 0x4f7ffffe, v6
	v_cvt_u32_f32_e32 v6, v6
	v_ashrrev_i32_e32 v8, 31, v8
	v_add_u32_e32 v2, v7, v2
	v_mul_lo_u32 v10, v10, v6
	v_mul_hi_u32 v10, v6, v10
	v_add_u32_e32 v6, v6, v10
	v_mul_hi_u32 v6, v9, v6
	v_mul_lo_u32 v10, v6, v5
	v_sub_u32_e32 v9, v9, v10
	v_add_u32_e32 v10, 1, v6
	v_sub_u32_e32 v11, v9, v5
	v_cmp_ge_u32_e32 vcc, v9, v5
	s_nop 1
	v_cndmask_b32_e32 v6, v6, v10, vcc
	v_cndmask_b32_e32 v9, v9, v11, vcc
	v_add_u32_e32 v10, 1, v6
	v_cmp_ge_u32_e32 vcc, v9, v5
	s_nop 1
	v_cndmask_b32_e32 v5, v6, v10, vcc
	v_xor_b32_e32 v5, v5, v8
	v_sub_u32_e32 v6, v5, v8
	v_mul_lo_u32 v3, v6, v3
	v_ashrrev_i32_e32 v7, 31, v6
	v_sub_u32_e32 v8, v2, v3
	v_mul_hi_u32 v3, v4, s6
	v_mul_lo_u32 v2, v4, s6
	v_lshlrev_b64 v[4:5], 19, v[6:7]
	v_lshl_add_u64 v[2:3], v[2:3], 0, v[4:5]
	v_lshlrev_b32_e32 v4, 8, v8
	v_lshlrev_b32_e32 v5, 8, v6
	s_mov_b64 s[6:7], -1
